# P10: alternate sweep direction per token (descending on odd tokens) + one workgroup barrier per token to keep the 8 waves of a CU on the same table window
# speedup vs baseline: 1.0171x; 1.0171x over previous
; #define LAS __attribute__((address_space(3)))
; __device__ __forceinline__ void expert_tokens(const unsigned char* __restrict__ UV, const float* __restrict__ US, const float* __restrict__ VS, ...
;     ...
;     for (int t = t0; t < t1; ++t) {
;         const bool has_next = t + 1 < t1; const int tn = has_next ? t + 1 : t;
;         const LAS float* pvt = pv; asm volatile("" : "+v"(pvt));
;         const unsigned nw0 = (unsigned)IDX[(size_t)tn * 128 + lane], nw1 = (unsigned)IDX[(size_t)tn * 128 + 64 + lane];
;         const int ni0 = (int)nw0 & rmask, ni1 = (int)nw1 & rmask;
;         const float ng0 = __uint_as_float(nw0 & 0xFFFF0000u), ng1 = __uint_as_float(nw1 & 0xFFFF0000u);
;         if (t == t0) asm volatile("s_waitcnt vmcnt(0)" ::: "memory"); else asm volatile("s_waitcnt vmcnt(32)" ::: "memory");
.LBB0_1014:
	s_barrier
	s_add_i32 s34, s20, 1
	s_cmp_ge_i32 s34, s17
	s_cselect_b64 s[18:19], -1, 0
	s_cmp_lt_i32 s34, s17
	s_cselect_b64 s[22:23], -1, 0
	s_and_b64 s[4:5], s[22:23], exec
	s_cselect_b32 s4, s34, s20
	s_ashr_i32 s5, s4, 31
	s_lshl_b64 s[24:25], s[4:5], 9
	v_mov_b32_e32 v0, 0
	v_lshl_add_u64 v[74:75], v[196:197], 0, s[24:25]
	global_load_dword v237, v[74:75], off
	global_load_dword v238, v[74:75], off offset:256
	s_cmp_lg_u32 s20, s8
	s_mov_b64 s[24:25], -1
	s_cbranch_scc0 .LBB0_1023
	s_waitcnt vmcnt(32)
	s_cbranch_execz .LBB0_1024

.LBB0_1019:
	v_mov_b32_e32 v88, 0
	v_dot8c_i32_i4_e32 v88, v248, v70
	v_dot8c_i32_i4_e32 v88, v250, v71
	v_mov_b32_e32 v74, 0
	v_mov_b32_e32 v75, 0
	v_mov_b32_e32 v76, 0
	v_lshlrev_b32_e32 v88, 4, v88
	v_mov_b32_e32 v77, 0
	v_mov_b32_e32 v78, 0
	v_mov_b32_e32 v79, 0
	v_mov_b32_e32 v80, 0
	v_mov_b32_e32 v81, 0
	v_mov_b32_e32 v82, 0
	v_mov_b32_e32 v83, 0
	v_mov_b32_e32 v84, 0
	v_mov_b32_e32 v85, 0
	v_mov_b32_e32 v86, 0
	v_mov_b32_e32 v87, 0
	v_dot8c_i32_i4_e32 v88, v247, v70
	v_mov_b32_e32 v70, 0
	v_dot8c_i32_i4_e32 v74, v248, v188
	v_dot8c_i32_i4_e32 v75, v248, v184
	v_dot8c_i32_i4_e32 v76, v248, v180
	v_dot8c_i32_i4_e32 v77, v248, v176
	v_dot8c_i32_i4_e32 v78, v248, v172
	v_dot8c_i32_i4_e32 v79, v248, v168
	v_dot8c_i32_i4_e32 v80, v248, v164
	v_dot8c_i32_i4_e32 v81, v248, v160
	v_dot8c_i32_i4_e32 v82, v248, v156
	v_dot8c_i32_i4_e32 v83, v248, v152
	v_dot8c_i32_i4_e32 v84, v248, v148
	v_dot8c_i32_i4_e32 v85, v248, v144
	v_dot8c_i32_i4_e32 v86, v248, v116
	v_dot8c_i32_i4_e32 v87, v248, v112
	v_dot8c_i32_i4_e32 v70, v248, v66
	v_dot8c_i32_i4_e32 v74, v250, v189
	v_dot8c_i32_i4_e32 v75, v250, v185
	v_dot8c_i32_i4_e32 v76, v250, v181
	v_dot8c_i32_i4_e32 v77, v250, v177
	v_dot8c_i32_i4_e32 v78, v250, v173
	v_dot8c_i32_i4_e32 v79, v250, v169
	v_dot8c_i32_i4_e32 v80, v250, v165
	v_dot8c_i32_i4_e32 v81, v250, v161
	v_dot8c_i32_i4_e32 v82, v250, v157
	v_dot8c_i32_i4_e32 v83, v250, v153
	v_dot8c_i32_i4_e32 v84, v250, v149
	v_dot8c_i32_i4_e32 v85, v250, v145
	v_dot8c_i32_i4_e32 v86, v250, v117
	v_dot8c_i32_i4_e32 v87, v250, v113
	v_dot8c_i32_i4_e32 v70, v250, v67
	v_lshlrev_b32_e32 v74, 4, v74
	v_lshlrev_b32_e32 v75, 4, v75
	v_lshlrev_b32_e32 v76, 4, v76
	v_lshlrev_b32_e32 v77, 4, v77
	v_lshlrev_b32_e32 v78, 4, v78
	v_lshlrev_b32_e32 v79, 4, v79
	v_lshlrev_b32_e32 v80, 4, v80
	v_lshlrev_b32_e32 v81, 4, v81
	v_lshlrev_b32_e32 v82, 4, v82
	v_lshlrev_b32_e32 v83, 4, v83
	v_lshlrev_b32_e32 v84, 4, v84
	v_lshlrev_b32_e32 v85, 4, v85
	v_lshlrev_b32_e32 v86, 4, v86
	v_lshlrev_b32_e32 v87, 4, v87
	v_lshlrev_b32_e32 v70, 4, v70
	v_dot8c_i32_i4_e32 v74, v247, v188
	v_dot8c_i32_i4_e32 v75, v247, v184
	v_dot8c_i32_i4_e32 v76, v247, v180
	v_dot8c_i32_i4_e32 v77, v247, v176
	v_dot8c_i32_i4_e32 v78, v247, v172
	v_dot8c_i32_i4_e32 v79, v247, v168
	v_dot8c_i32_i4_e32 v80, v247, v164
	v_dot8c_i32_i4_e32 v81, v247, v160
	v_dot8c_i32_i4_e32 v82, v247, v156
	v_dot8c_i32_i4_e32 v83, v247, v152
	v_dot8c_i32_i4_e32 v84, v247, v148
	v_dot8c_i32_i4_e32 v85, v247, v144
	v_dot8c_i32_i4_e32 v86, v247, v116
	v_dot8c_i32_i4_e32 v87, v247, v112
	v_dot8c_i32_i4_e32 v70, v247, v66
	v_dot8c_i32_i4_e32 v74, v249, v189
	v_dot8c_i32_i4_e32 v75, v249, v185
	v_dot8c_i32_i4_e32 v76, v249, v181
	v_dot8c_i32_i4_e32 v77, v249, v177
	v_dot8c_i32_i4_e32 v78, v249, v173
	v_dot8c_i32_i4_e32 v79, v249, v169
	v_dot8c_i32_i4_e32 v80, v249, v165
	v_dot8c_i32_i4_e32 v81, v249, v161
	v_dot8c_i32_i4_e32 v82, v249, v157
	v_dot8c_i32_i4_e32 v83, v249, v153
	v_dot8c_i32_i4_e32 v84, v249, v149
	v_dot8c_i32_i4_e32 v85, v249, v145
	v_dot8c_i32_i4_e32 v86, v249, v117
	v_dot8c_i32_i4_e32 v87, v249, v113
	v_dot8c_i32_i4_e32 v88, v249, v71
	v_dot8c_i32_i4_e32 v70, v249, v67
	v_permlane32_swap_b32_e32 v74, v82
	v_permlane32_swap_b32_e32 v75, v83
	v_permlane32_swap_b32_e32 v76, v84
	v_permlane32_swap_b32_e32 v77, v85
	v_permlane32_swap_b32_e32 v78, v86
	v_permlane32_swap_b32_e32 v79, v87
	v_permlane32_swap_b32_e32 v80, v88
	v_permlane32_swap_b32_e32 v81, v70
	v_add_u32_e32 v66, v74, v82
	v_add_u32_e32 v67, v75, v83
	v_add_u32_e32 v71, v76, v84
	v_add_u32_e32 v74, v77, v85
	v_add_u32_e32 v75, v78, v86
	v_add_u32_e32 v76, v79, v87
	v_add_u32_e32 v77, v80, v88
	v_add_u32_e32 v70, v81, v70
	v_permlane16_swap_b32_e32 v66, v75
	v_permlane16_swap_b32_e32 v67, v76
	v_permlane16_swap_b32_e32 v71, v77
	v_permlane16_swap_b32_e32 v74, v70
	v_add_u32_e32 v66, v66, v75
	v_add_u32_e32 v67, v67, v76
	v_add_u32_e32 v71, v71, v77
	v_add_u32_e32 v70, v74, v70
	v_cndmask_b32_e64 v74, v71, v66, s[0:1]
	v_cndmask_b32_e64 v66, v66, v71, s[0:1]
	v_cndmask_b32_e64 v71, v70, v67, s[0:1]
	v_cndmask_b32_e64 v67, v67, v70, s[0:1]
	v_add_u32_dpp v66, v66, v74 quad_perm:[2,3,0,1] row_mask:0xf bank_mask:0xf bound_ctrl:1
	s_sub_i32 s4, s21, 32
	v_add_u32_dpp v67, v67, v71 quad_perm:[2,3,0,1] row_mask:0xf bank_mask:0xf bound_ctrl:1
	v_cndmask_b32_e64 v70, v67, v66, s[2:3]
	v_cndmask_b32_e64 v66, v66, v67, s[2:3]
	s_cmp_lt_u32 s25, 4
	s_cselect_b64 vcc, -1, 0
	v_add_u32_dpp v66, v66, v70 quad_perm:[1,0,3,2] row_mask:0xf bank_mask:0xf bound_ctrl:1
	v_cndmask_b32_e32 v70, v234, v233, vcc
	v_cndmask_b32_e32 v71, v230, v229, vcc
	v_add_u32_dpp v66, v66, v66 row_ror:8 row_mask:0xf bank_mask:0xf bound_ctrl:1
	s_cmp_eq_u32 s21, 32
	s_nop 0
	v_add_u32_dpp v67, v66, v66 row_ror:4 row_mask:0xf bank_mask:0xf bound_ctrl:1
	v_and_or_b32 v66, s4, 32, v193
	v_lshlrev_b32_e32 v66, 2, v66
	v_cvt_f32_i32_e32 v74, v67
	ds_bpermute_b32 v75, v66, v70
	v_and_b32_e32 v67, 0xffff0000, v71
	ds_bpermute_b32 v76, v66, v67
	v_add_f32_e32 v71, v251, v74
	v_mul_f32_e32 v71, v244, v71
	s_waitcnt lgkmcnt(1)
	v_mul_f32_e32 v74, v71, v75
	v_fma_f32 v71, |v74|, s28, 1.0
	v_rcp_f32_e32 v75, v71
	v_mul_f32_e32 v79, v74, v74
	v_mul_f32_e32 v79, 0xbf38aa3b, v79
	v_exp_f32_e32 v79, v79
	v_fmamk_f32 v78, v75, 0x3f07dc22, v227
	v_fmaak_f32 v78, v75, v78, 0x3f35f0e3
	v_fmaak_f32 v78, v75, v78, 0xbe11a98e
	v_cndmask_b32_e32 v71, v236, v235, vcc
	v_fmaak_f32 v78, v75, v78, 0x3e027906
	ds_bpermute_b32 v77, v66, v71
	v_mul_f32_e32 v75, v75, v78
	v_mul_f32_e32 v75, v79, v75
	v_mul_f32_e32 v78, v74, v75
	v_fma_f32 v75, -v74, v75, v74
	v_cmp_gt_f32_e32 vcc, 0, v74
	s_nop 1
	v_cndmask_b32_e32 v74, v75, v78, vcc
	s_waitcnt lgkmcnt(1)
	v_mul_f32_e32 v74, v74, v76
	s_cselect_b64 vcc, -1, 0
	s_cmp_gt_u32 s25, 5
	s_waitcnt lgkmcnt(0)
	v_mul_f32_e32 v74, v74, v77
	s_cselect_b64 s[22:23], -1, 0
	s_cmp_lt_u32 s25, 6
	v_fma_mixlo_f16 v116, v74, s16, 0
	s_cselect_b64 s[4:5], -1, 0
	v_and_b32_e32 v117, 0xffff, v116
	v_cndmask_b32_e64 v74, v242, v232, s[4:5]
	s_add_i32 s24, s21, 1
	s_add_i32 s35, s21, 2
	s_add_i32 s36, s21, 3
	s_add_i32 s37, s21, 4
	s_add_i32 s38, s21, 5
	s_add_i32 s39, s21, 6
	s_add_i32 s40, s21, 7
	s_add_i32 s49, s21, 8
	s_add_i32 s50, s21, 9
	s_add_i32 s51, s21, 10
	s_add_i32 s52, s21, 11
	s_add_i32 s53, s21, 12
	s_add_i32 s54, s21, 13
	s_add_i32 s55, s21, 14
	s_add_i32 s56, s21, 15
	v_cndmask_b32_e32 v136, v74, v231, vcc
	v_readlane_b32 s47, v117, 0
	v_readlane_b32 s48, v117, 1
	s_cmp_lg_u32 s21, 32
	v_readlane_b32 s4, v136, s21
	s_nop 1
	v_lshl_or_b32 v74, s4, 10, v194
	v_readlane_b32 s4, v136, s24
	s_nop 1
	v_lshl_or_b32 v75, s4, 10, v194
	global_load_dwordx4 v[78:81], v74, s[10:11]
	s_nop 0
	global_load_dwordx4 v[74:77], v75, s[10:11]
	v_readlane_b32 s45, v117, 2
	v_readlane_b32 s46, v117, 3
	v_readlane_b32 s4, v136, s35
	s_nop 1
	v_lshl_or_b32 v82, s4, 10, v194
	v_readlane_b32 s4, v136, s36
	s_nop 1
	v_lshl_or_b32 v83, s4, 10, v194
	global_load_dwordx4 v[86:89], v82, s[10:11]
	s_nop 0
	global_load_dwordx4 v[82:85], v83, s[10:11]
	v_readlane_b32 s43, v117, 16
	v_readlane_b32 s44, v117, 17
	v_readlane_b32 s4, v136, s37
	s_nop 1
	v_lshl_or_b32 v90, s4, 10, v194
	v_readlane_b32 s4, v136, s38
	s_nop 1
	v_lshl_or_b32 v91, s4, 10, v194
	global_load_dwordx4 v[94:97], v90, s[10:11]
	s_nop 0
	global_load_dwordx4 v[90:93], v91, s[10:11]
	v_readlane_b32 s41, v117, 18
	v_readlane_b32 s42, v117, 19
	v_readlane_b32 s4, v136, s39
	s_nop 1
	v_lshl_or_b32 v98, s4, 10, v194
	v_readlane_b32 s4, v136, s40
	s_nop 1
	v_lshl_or_b32 v99, s4, 10, v194
	global_load_dwordx4 v[102:105], v98, s[10:11]
	s_nop 0
	global_load_dwordx4 v[98:101], v99, s[10:11]
	v_readlane_b32 s39, v117, 32
	v_readlane_b32 s40, v117, 33
	v_readlane_b32 s4, v136, s49
	s_nop 1
	v_lshl_or_b32 v106, s4, 10, v194
	v_readlane_b32 s4, v136, s50
	s_nop 1
	v_lshl_or_b32 v107, s4, 10, v194
	global_load_dwordx4 v[110:113], v106, s[10:11]
	s_nop 0
	global_load_dwordx4 v[106:109], v107, s[10:11]
	v_readlane_b32 s37, v117, 34
	v_readlane_b32 s38, v117, 35
	v_readlane_b32 s4, v136, s51
	s_nop 1
	v_lshl_or_b32 v120, s4, 10, v194
	v_readlane_b32 s4, v136, s52
	s_nop 1
	v_lshl_or_b32 v121, s4, 10, v194
	global_load_dwordx4 v[124:127], v120, s[10:11]
	s_nop 0
	global_load_dwordx4 v[120:123], v121, s[10:11]
	v_readlane_b32 s35, v117, 48
	v_readlane_b32 s36, v117, 49
	v_readlane_b32 s4, v136, s53
	s_nop 1
	v_lshl_or_b32 v128, s4, 10, v194
	v_readlane_b32 s4, v136, s54
	s_nop 1
	v_lshl_or_b32 v129, s4, 10, v194
	global_load_dwordx4 v[132:135], v128, s[10:11]
	s_nop 0
	global_load_dwordx4 v[128:131], v129, s[10:11]
	v_readlane_b32 s4, v117, 50
	v_readlane_b32 s5, v117, 51
	v_readlane_b32 s24, v136, s55
	s_nop 1
	v_lshl_or_b32 v117, s24, 10, v194
	v_readlane_b32 s24, v136, s56
	s_nop 1
	v_lshl_or_b32 v136, s24, 10, v194
	global_load_dwordx4 v[140:143], v117, s[10:11]
	s_nop 0
	global_load_dwordx4 v[136:139], v136, s[10:11]
	s_cbranch_scc1 .LBB0_1021
	s_waitcnt vmcnt(16)
	s_bfe_i32 s60, s34, 0x10000
	v_alignbit_b32 v237, v237, v237, 16
	v_alignbit_b32 v238, v238, v238, 16
	v_xor_b32_e32 v237, s60, v237
	v_xor_b32_e32 v238, s60, v238
	s_nop 1
	s_mov_b32 s58, 0x99999999
	s_mov_b32 s59, 0x99999999
	v_min_u32_dpp v202, v237, v237 quad_perm:[1,0,3,2] row_mask:0xf bank_mask:0xf
	v_max_u32_dpp v203, v237, v237 quad_perm:[1,0,3,2] row_mask:0xf bank_mask:0xf
	v_min_u32_dpp v204, v238, v238 quad_perm:[1,0,3,2] row_mask:0xf bank_mask:0xf
	v_max_u32_dpp v205, v238, v238 quad_perm:[1,0,3,2] row_mask:0xf bank_mask:0xf
	v_cndmask_b32_e64 v237, v203, v202, s[58:59]
	v_cndmask_b32_e64 v238, v205, v204, s[58:59]
	s_mov_b32 s58, 0xcc33cc33
	s_mov_b32 s59, 0xcc33cc33
	v_min_u32_dpp v202, v237, v237 quad_perm:[2,3,0,1] row_mask:0xf bank_mask:0xf
	v_max_u32_dpp v203, v237, v237 quad_perm:[2,3,0,1] row_mask:0xf bank_mask:0xf
	v_min_u32_dpp v204, v238, v238 quad_perm:[2,3,0,1] row_mask:0xf bank_mask:0xf
	v_max_u32_dpp v205, v238, v238 quad_perm:[2,3,0,1] row_mask:0xf bank_mask:0xf
	v_cndmask_b32_e64 v237, v203, v202, s[58:59]
	v_cndmask_b32_e64 v238, v205, v204, s[58:59]
	s_mov_b32 s58, 0xaa55aa55
	s_mov_b32 s59, 0xaa55aa55
	v_min_u32_dpp v202, v237, v237 quad_perm:[1,0,3,2] row_mask:0xf bank_mask:0xf
	v_max_u32_dpp v203, v237, v237 quad_perm:[1,0,3,2] row_mask:0xf bank_mask:0xf
	v_min_u32_dpp v204, v238, v238 quad_perm:[1,0,3,2] row_mask:0xf bank_mask:0xf
	v_max_u32_dpp v205, v238, v238 quad_perm:[1,0,3,2] row_mask:0xf bank_mask:0xf
	v_cndmask_b32_e64 v237, v203, v202, s[58:59]
	v_cndmask_b32_e64 v238, v205, v204, s[58:59]
	s_mov_b32 s58, 0xf00ff00f
	s_mov_b32 s59, 0xf00ff00f
	v_min_u32_dpp v202, v237, v237 row_ror:8 row_mask:0xf bank_mask:0xf
	v_max_u32_dpp v203, v237, v237 row_ror:8 row_mask:0xf bank_mask:0xf
	v_min_u32_dpp v204, v238, v238 row_ror:8 row_mask:0xf bank_mask:0xf
	v_max_u32_dpp v205, v238, v238 row_ror:8 row_mask:0xf bank_mask:0xf
	v_cndmask_b32_e64 v237, v203, v202, s[58:59]
	v_cndmask_b32_e64 v238, v205, v204, s[58:59]
	s_mov_b32 s58, 0xc3c3c3c3
	s_mov_b32 s59, 0xc3c3c3c3
	v_min_u32_dpp v202, v237, v237 quad_perm:[2,3,0,1] row_mask:0xf bank_mask:0xf
	v_max_u32_dpp v203, v237, v237 quad_perm:[2,3,0,1] row_mask:0xf bank_mask:0xf
	v_min_u32_dpp v204, v238, v238 quad_perm:[2,3,0,1] row_mask:0xf bank_mask:0xf
	v_max_u32_dpp v205, v238, v238 quad_perm:[2,3,0,1] row_mask:0xf bank_mask:0xf
	v_cndmask_b32_e64 v237, v203, v202, s[58:59]
; __device__ __forceinline__ void expert_tokens(const unsigned char* __restrict__ UV, const float* __restrict__ US, const float* __restrict__ VS, ...
;     ...
;         const unsigned nw0 = (unsigned)IDX[(size_t)tn * 128 + lane], nw1 = (unsigned)IDX[(size_t)tn * 128 + 64 + lane];
;         const int ni0 = (int)nw0 & rmask, ni1 = (int)nw1 & rmask;
	v_cndmask_b32_e64 v238, v205, v204, s[58:59]
	s_mov_b32 s58, 0xa5a5a5a5
	s_mov_b32 s59, 0xa5a5a5a5
	v_min_u32_dpp v202, v237, v237 quad_perm:[1,0,3,2] row_mask:0xf bank_mask:0xf
	v_max_u32_dpp v203, v237, v237 quad_perm:[1,0,3,2] row_mask:0xf bank_mask:0xf
	v_min_u32_dpp v204, v238, v238 quad_perm:[1,0,3,2] row_mask:0xf bank_mask:0xf
	v_max_u32_dpp v205, v238, v238 quad_perm:[1,0,3,2] row_mask:0xf bank_mask:0xf
	v_cndmask_b32_e64 v237, v203, v202, s[58:59]
	v_cndmask_b32_e64 v238, v205, v204, s[58:59]
	s_mov_b32 s58, 0xf0f00f0f
	s_mov_b32 s59, 0xf0f00f0f
	v_mov_b32_dpp v202, v237 row_half_mirror row_mask:0xf bank_mask:0xf
	v_mov_b32_dpp v204, v238 row_half_mirror row_mask:0xf bank_mask:0xf
	s_nop 0
	v_max_u32_dpp v203, v202, v237 quad_perm:[3,2,1,0] row_mask:0xf bank_mask:0xf
	v_max_u32_dpp v205, v204, v238 quad_perm:[3,2,1,0] row_mask:0xf bank_mask:0xf
	v_min_u32_dpp v202, v202, v237 quad_perm:[3,2,1,0] row_mask:0xf bank_mask:0xf
	v_min_u32_dpp v204, v204, v238 quad_perm:[3,2,1,0] row_mask:0xf bank_mask:0xf
	v_cndmask_b32_e64 v237, v203, v202, s[58:59]
	v_cndmask_b32_e64 v238, v205, v204, s[58:59]
	s_mov_b32 s58, 0xff0000ff
	s_mov_b32 s59, 0xff0000ff
	v_min_u32_dpp v202, v237, v237 row_ror:8 row_mask:0xf bank_mask:0xf
	v_max_u32_dpp v203, v237, v237 row_ror:8 row_mask:0xf bank_mask:0xf
	v_min_u32_dpp v204, v238, v238 row_ror:8 row_mask:0xf bank_mask:0xf
	v_max_u32_dpp v205, v238, v238 row_ror:8 row_mask:0xf bank_mask:0xf
	v_cndmask_b32_e64 v237, v203, v202, s[58:59]
	v_cndmask_b32_e64 v238, v205, v204, s[58:59]
	s_mov_b32 s58, 0xcccc3333
	s_mov_b32 s59, 0xcccc3333
	v_min_u32_dpp v202, v237, v237 quad_perm:[2,3,0,1] row_mask:0xf bank_mask:0xf
	v_max_u32_dpp v203, v237, v237 quad_perm:[2,3,0,1] row_mask:0xf bank_mask:0xf
	v_min_u32_dpp v204, v238, v238 quad_perm:[2,3,0,1] row_mask:0xf bank_mask:0xf
	v_max_u32_dpp v205, v238, v238 quad_perm:[2,3,0,1] row_mask:0xf bank_mask:0xf
	v_cndmask_b32_e64 v237, v203, v202, s[58:59]
	v_cndmask_b32_e64 v238, v205, v204, s[58:59]
	s_mov_b32 s58, 0xaaaa5555
	s_mov_b32 s59, 0xaaaa5555
	v_min_u32_dpp v202, v237, v237 quad_perm:[1,0,3,2] row_mask:0xf bank_mask:0xf
	v_max_u32_dpp v203, v237, v237 quad_perm:[1,0,3,2] row_mask:0xf bank_mask:0xf
	v_min_u32_dpp v204, v238, v238 quad_perm:[1,0,3,2] row_mask:0xf bank_mask:0xf
	v_max_u32_dpp v205, v238, v238 quad_perm:[1,0,3,2] row_mask:0xf bank_mask:0xf
	v_cndmask_b32_e64 v237, v203, v202, s[58:59]
	v_cndmask_b32_e64 v238, v205, v204, s[58:59]
	s_nop 1
	v_permlane16_swap_b32_e32 v237, v238
	s_mov_b32 s58, -1
	s_mov_b32 s59, 0
	v_min_u32_e32 v202, v237, v238
	v_max_u32_e32 v203, v237, v238
	v_cndmask_b32_e64 v237, v203, v202, s[58:59]
	v_cndmask_b32_e64 v238, v202, v203, s[58:59]
	s_mov_b32 s58, 0xf0f0f0f
	s_mov_b32 s59, 0xf0f0f0f0
	v_mov_b32_dpp v202, v237 row_half_mirror row_mask:0xf bank_mask:0xf
	v_mov_b32_dpp v204, v238 row_half_mirror row_mask:0xf bank_mask:0xf
	s_nop 0
	v_max_u32_dpp v203, v202, v237 quad_perm:[3,2,1,0] row_mask:0xf bank_mask:0xf
	v_max_u32_dpp v205, v204, v238 quad_perm:[3,2,1,0] row_mask:0xf bank_mask:0xf
	v_min_u32_dpp v202, v202, v237 quad_perm:[3,2,1,0] row_mask:0xf bank_mask:0xf
	v_min_u32_dpp v204, v204, v238 quad_perm:[3,2,1,0] row_mask:0xf bank_mask:0xf
	v_cndmask_b32_e64 v237, v203, v202, s[58:59]
	v_cndmask_b32_e64 v238, v205, v204, s[58:59]
	s_mov_b32 s58, 0xff00ff
	s_mov_b32 s59, 0xff00ff00
	v_min_u32_dpp v202, v237, v237 row_ror:8 row_mask:0xf bank_mask:0xf
	v_max_u32_dpp v203, v237, v237 row_ror:8 row_mask:0xf bank_mask:0xf
	v_min_u32_dpp v204, v238, v238 row_ror:8 row_mask:0xf bank_mask:0xf
	v_max_u32_dpp v205, v238, v238 row_ror:8 row_mask:0xf bank_mask:0xf
	v_cndmask_b32_e64 v237, v203, v202, s[58:59]
	v_cndmask_b32_e64 v238, v205, v204, s[58:59]
	s_mov_b32 s58, 0x33333333
	s_mov_b32 s59, 0xcccccccc
	v_min_u32_dpp v202, v237, v237 quad_perm:[2,3,0,1] row_mask:0xf bank_mask:0xf
	v_max_u32_dpp v203, v237, v237 quad_perm:[2,3,0,1] row_mask:0xf bank_mask:0xf
	v_min_u32_dpp v204, v238, v238 quad_perm:[2,3,0,1] row_mask:0xf bank_mask:0xf
	v_max_u32_dpp v205, v238, v238 quad_perm:[2,3,0,1] row_mask:0xf bank_mask:0xf
	v_cndmask_b32_e64 v237, v203, v202, s[58:59]
	v_cndmask_b32_e64 v238, v205, v204, s[58:59]
	s_mov_b32 s58, 0x55555555
	s_mov_b32 s59, 0xaaaaaaaa
	v_min_u32_dpp v202, v237, v237 quad_perm:[1,0,3,2] row_mask:0xf bank_mask:0xf
	v_max_u32_dpp v203, v237, v237 quad_perm:[1,0,3,2] row_mask:0xf bank_mask:0xf
	v_min_u32_dpp v204, v238, v238 quad_perm:[1,0,3,2] row_mask:0xf bank_mask:0xf
	v_max_u32_dpp v205, v238, v238 quad_perm:[1,0,3,2] row_mask:0xf bank_mask:0xf
	v_cndmask_b32_e64 v237, v203, v202, s[58:59]
	v_cndmask_b32_e64 v238, v205, v204, s[58:59]
	s_nop 1
	v_permlane32_swap_b32_e32 v237, v238
	s_mov_b32 s58, 0xffff
	s_mov_b32 s59, 0xffff
	v_min_u32_e32 v202, v237, v238
	v_max_u32_e32 v203, v237, v238
	v_cndmask_b32_e64 v237, v203, v202, s[58:59]
	v_cndmask_b32_e64 v238, v202, v203, s[58:59]
	s_nop 1
	v_permlane32_swap_b32_e32 v237, v238
	s_mov_b32 s58, 0xffff
	s_mov_b32 s59, 0xffff
; __device__ __forceinline__ void expert_tokens(const unsigned char* __restrict__ UV, const float* __restrict__ US, const float* __restrict__ VS, ...
;     ...
;         const int ni0 = (int)nw0 & rmask, ni1 = (int)nw1 & rmask;
;         const float ng0 = __uint_as_float(nw0 & 0xFFFF0000u), ng1 = __uint_as_float(nw1 & 0xFFFF0000u);
;     ...
;             if (bi == 0) { nsu0 = US[ni0]; nsu1 = US[ni1]; nsv0 = VS[ni0]; nsv1 = VS[ni1]; }
	v_min_u32_e32 v202, v237, v238
	v_max_u32_e32 v203, v237, v238
	v_cndmask_b32_e64 v237, v203, v202, s[58:59]
	v_cndmask_b32_e64 v238, v202, v203, s[58:59]
	s_mov_b32 s58, 0xf0f00f0f
	s_mov_b32 s59, 0xf0f00f0f
	v_mov_b32_dpp v202, v237 row_half_mirror row_mask:0xf bank_mask:0xf
	v_mov_b32_dpp v204, v238 row_half_mirror row_mask:0xf bank_mask:0xf
	s_nop 0
	v_max_u32_dpp v203, v202, v237 quad_perm:[3,2,1,0] row_mask:0xf bank_mask:0xf
	v_max_u32_dpp v205, v204, v238 quad_perm:[3,2,1,0] row_mask:0xf bank_mask:0xf
	v_min_u32_dpp v202, v202, v237 quad_perm:[3,2,1,0] row_mask:0xf bank_mask:0xf
	v_min_u32_dpp v204, v204, v238 quad_perm:[3,2,1,0] row_mask:0xf bank_mask:0xf
	v_cndmask_b32_e64 v237, v203, v202, s[58:59]
	v_cndmask_b32_e64 v238, v205, v204, s[58:59]
	s_mov_b32 s58, 0xff0000ff
	s_mov_b32 s59, 0xff0000ff
	v_min_u32_dpp v202, v237, v237 row_ror:8 row_mask:0xf bank_mask:0xf
	v_max_u32_dpp v203, v237, v237 row_ror:8 row_mask:0xf bank_mask:0xf
	v_min_u32_dpp v204, v238, v238 row_ror:8 row_mask:0xf bank_mask:0xf
	v_max_u32_dpp v205, v238, v238 row_ror:8 row_mask:0xf bank_mask:0xf
	v_cndmask_b32_e64 v237, v203, v202, s[58:59]
	v_cndmask_b32_e64 v238, v205, v204, s[58:59]
	s_mov_b32 s58, 0xcccc3333
	s_mov_b32 s59, 0xcccc3333
	v_min_u32_dpp v202, v237, v237 quad_perm:[2,3,0,1] row_mask:0xf bank_mask:0xf
	v_max_u32_dpp v203, v237, v237 quad_perm:[2,3,0,1] row_mask:0xf bank_mask:0xf
	v_min_u32_dpp v204, v238, v238 quad_perm:[2,3,0,1] row_mask:0xf bank_mask:0xf
	v_max_u32_dpp v205, v238, v238 quad_perm:[2,3,0,1] row_mask:0xf bank_mask:0xf
	v_cndmask_b32_e64 v237, v203, v202, s[58:59]
	v_cndmask_b32_e64 v238, v205, v204, s[58:59]
	s_mov_b32 s58, 0xaaaa5555
	s_mov_b32 s59, 0xaaaa5555
	v_min_u32_dpp v202, v237, v237 quad_perm:[1,0,3,2] row_mask:0xf bank_mask:0xf
	v_max_u32_dpp v203, v237, v237 quad_perm:[1,0,3,2] row_mask:0xf bank_mask:0xf
	v_min_u32_dpp v204, v238, v238 quad_perm:[1,0,3,2] row_mask:0xf bank_mask:0xf
	v_max_u32_dpp v205, v238, v238 quad_perm:[1,0,3,2] row_mask:0xf bank_mask:0xf
	v_cndmask_b32_e64 v237, v203, v202, s[58:59]
	v_cndmask_b32_e64 v238, v205, v204, s[58:59]
	s_nop 1
	v_permlane16_swap_b32_e32 v237, v238
	v_min_u32_e32 v202, v237, v238
	v_max_u32_e32 v238, v237, v238
	v_mov_b32_e32 v237, v202
	s_nop 1
	v_permlane32_swap_b32_e32 v237, v238
	v_min_u32_e32 v202, v237, v238
	v_max_u32_e32 v238, v237, v238
	v_mov_b32_e32 v237, v202
	s_nop 1
	v_permlane16_swap_b32_e32 v237, v238
	v_min_u32_e32 v202, v237, v238
	v_max_u32_e32 v238, v237, v238
	v_mov_b32_e32 v237, v202
	s_mov_b32 s58, 0xf0f0f0f
	s_mov_b32 s59, 0xf0f0f0f
	v_mov_b32_dpp v202, v237 row_half_mirror row_mask:0xf bank_mask:0xf
	v_mov_b32_dpp v204, v238 row_half_mirror row_mask:0xf bank_mask:0xf
	s_nop 0
	v_max_u32_dpp v203, v202, v237 quad_perm:[3,2,1,0] row_mask:0xf bank_mask:0xf
	v_max_u32_dpp v205, v204, v238 quad_perm:[3,2,1,0] row_mask:0xf bank_mask:0xf
	v_min_u32_dpp v202, v202, v237 quad_perm:[3,2,1,0] row_mask:0xf bank_mask:0xf
	v_min_u32_dpp v204, v204, v238 quad_perm:[3,2,1,0] row_mask:0xf bank_mask:0xf
	v_cndmask_b32_e64 v237, v203, v202, s[58:59]
	v_cndmask_b32_e64 v238, v205, v204, s[58:59]
	s_mov_b32 s58, 0xff00ff
	s_mov_b32 s59, 0xff00ff
	v_min_u32_dpp v202, v237, v237 row_ror:8 row_mask:0xf bank_mask:0xf
	v_max_u32_dpp v203, v237, v237 row_ror:8 row_mask:0xf bank_mask:0xf
	v_min_u32_dpp v204, v238, v238 row_ror:8 row_mask:0xf bank_mask:0xf
	v_max_u32_dpp v205, v238, v238 row_ror:8 row_mask:0xf bank_mask:0xf
	v_cndmask_b32_e64 v237, v203, v202, s[58:59]
	v_cndmask_b32_e64 v238, v205, v204, s[58:59]
	s_mov_b32 s58, 0x33333333
	s_mov_b32 s59, 0x33333333
	v_min_u32_dpp v202, v237, v237 quad_perm:[2,3,0,1] row_mask:0xf bank_mask:0xf
	v_max_u32_dpp v203, v237, v237 quad_perm:[2,3,0,1] row_mask:0xf bank_mask:0xf
	v_min_u32_dpp v204, v238, v238 quad_perm:[2,3,0,1] row_mask:0xf bank_mask:0xf
	v_max_u32_dpp v205, v238, v238 quad_perm:[2,3,0,1] row_mask:0xf bank_mask:0xf
	v_cndmask_b32_e64 v237, v203, v202, s[58:59]
	v_cndmask_b32_e64 v238, v205, v204, s[58:59]
	s_mov_b32 s58, 0x55555555
	s_mov_b32 s59, 0x55555555
	v_min_u32_dpp v202, v237, v237 quad_perm:[1,0,3,2] row_mask:0xf bank_mask:0xf
	v_max_u32_dpp v203, v237, v237 quad_perm:[1,0,3,2] row_mask:0xf bank_mask:0xf
	v_min_u32_dpp v204, v238, v238 quad_perm:[1,0,3,2] row_mask:0xf bank_mask:0xf
	v_max_u32_dpp v205, v238, v238 quad_perm:[1,0,3,2] row_mask:0xf bank_mask:0xf
	v_cndmask_b32_e64 v237, v203, v202, s[58:59]
	v_cndmask_b32_e64 v238, v205, v204, s[58:59]
	s_nop 1
	v_permlane16_swap_b32_e32 v237, v238
	s_nop 1
	v_permlane32_swap_b32_e32 v237, v238
	v_xor_b32_e32 v237, s60, v237
	v_xor_b32_e32 v238, s60, v238
	v_alignbit_b32 v237, v237, v237, 16
	v_alignbit_b32 v238, v238, v238, 16
	v_and_b32_e32 v242, 0x3fff, v237
	v_and_b32_e32 v243, 0x3fff, v238
	v_lshlrev_b32_e32 v208, 2, v242
	v_lshlrev_b32_e32 v206, 2, v243
	global_load_dword v241, v208, s[12:13]
	global_load_dword v0, v206, s[12:13]
	global_load_dword v245, v208, s[14:15]
	global_load_dword v246, v206, s[14:15]
